# scan compute waves: S loop back edge waits lgkmcnt(2) (K fragments only) instead of draining the S-tile stores
# speedup vs baseline: 1.0174x; 1.0001x over previous
; #define LAS __attribute__((address_space(3)))
; #define LDS_WAIT() asm volatile("s_waitcnt lgkmcnt(0)" ::: "memory")
; __device__ __forceinline__ void p4_scan(const Args& a, const Frame& F) {
;     ...
;                     for (int pr = 0; pr < npB; ++pr) {
;                         LDS_WAIT(); __builtin_amdgcn_sched_barrier(0);
;                         const bool doA = pr < npA;
;                         f32x4 apA[2], apB[2], glv[2];
; #pragma unroll
;                         for (int u = 0; u < 2; ++u) glv[u] = *(const LAS f32x4*)(GL + 16 * (2 * pr + u) + 4 * q);
; #pragma unroll
;                         for (int u = 0; u < 2; ++u) { apA[u] = (f32x4){0.f, 0.f, 0.f, 0.f}; apB[u] = (f32x4){0.f, 0.f, 0.f, 0.f};
; #pragma unroll
;                             for (int ks = 0; ks < 4; ++ks) apB[u] = __builtin_amdgcn_mfma_f32_16x16x32_bf16(kf[u][ks], qfB[ks], apB[u], 0, 0, 0);
;                             if (doA) {
; #pragma unroll
;                                 for (int ks = 0; ks < 4; ++ks) apA[u] = __builtin_amdgcn_mfma_f32_16x16x32_bf16(kf[u][ks], qfA[ks], apA[u], 0, 0, 0); } }
;                         __builtin_amdgcn_sched_barrier(0);
;                         if (pr + 1 < npB) {
; #pragma unroll
;                             for (int u = 0; u < 2; ++u)
; #pragma unroll
;                                 for (int ks = 0; ks < 4; ++ks) kf[u][ks] = *(const LAS bf16x8*)(L + kcur + (16 * (2 * pr + 2 + u) + c) * SP + (ks * 32 + q * 8) * 2);
;                         }
.LBB0_456:
	v_add_u32_e32 v55, 32, v55
	v_add_u32_e32 v54, 64, v54
	v_add_u32_e32 v51, 64, v51
	v_add_u32_e32 v49, 0x2200, v49
	s_cmp_eq_u32 s79, s86
	v_add_u32_e32 v50, 0x80, v50
	s_cbranch_scc1 .LBB0_467
	s_waitcnt lgkmcnt(2)
	s_branch .Ls457b

; #define LAS __attribute__((address_space(3)))
; #define LDS_WAIT() asm volatile("s_waitcnt lgkmcnt(0)" ::: "memory")
; __device__ __forceinline__ void p4_scan(const Args& a, const Frame& F) {
;     ...
;                     for (int pr = 0; pr < npB; ++pr) {
;                         LDS_WAIT(); __builtin_amdgcn_sched_barrier(0);
;                         const bool doA = pr < npA;
;                         f32x4 apA[2], apB[2], glv[2];
; #pragma unroll
;                         for (int u = 0; u < 2; ++u) glv[u] = *(const LAS f32x4*)(GL + 16 * (2 * pr + u) + 4 * q);
; #pragma unroll
;                         for (int u = 0; u < 2; ++u) { apA[u] = (f32x4){0.f, 0.f, 0.f, 0.f}; apB[u] = (f32x4){0.f, 0.f, 0.f, 0.f};
; #pragma unroll
;                             for (int ks = 0; ks < 4; ++ks) apB[u] = __builtin_amdgcn_mfma_f32_16x16x32_bf16(kf[u][ks], qfB[ks], apB[u], 0, 0, 0);
;                             if (doA) {
; #pragma unroll
;                                 for (int ks = 0; ks < 4; ++ks) apA[u] = __builtin_amdgcn_mfma_f32_16x16x32_bf16(kf[u][ks], qfA[ks], apA[u], 0, 0, 0); } }
;                         __builtin_amdgcn_sched_barrier(0);
.Ls457b:
	v_mfma_f32_16x16x32_bf16 v[124:127], v[96:99], v[64:67], 0
	v_add_u32_e32 v120, 0, v50
	v_add_u32_e32 v121, 0x23430, v120
	v_add_u32_e32 v120, 0x23470, v120
	v_mfma_f32_16x16x32_bf16 v[124:127], v[92:95], v[68:71], v[124:127]
	ds_read_b128 v[128:131], v121
	ds_read_b128 v[120:123], v120
	s_cmp_lt_u32 s86, s78
	v_mfma_f32_16x16x32_bf16 v[124:127], v[88:91], v[80:83], v[124:127]
	s_cselect_b64 s[52:53], -1, 0
	s_and_b64 vcc, exec, s[52:53]
	v_mov_b32_e32 v136, 0
	v_mfma_f32_16x16x32_bf16 v[140:143], v[100:103], v[84:87], v[124:127]
	v_mov_b32_e32 v137, 0
	v_mov_b32_e32 v138, 0
	v_mov_b32_e32 v139, 0
	s_nop 0
	v_mov_b32_e32 v124, 0
	s_cbranch_vccz .LBB0_459
	v_mfma_f32_16x16x32_bf16 v[132:135], v[96:99], v[56:59], 0
	v_mfma_f32_16x16x32_bf16 v[132:135], v[92:95], v[60:63], v[132:135]
	v_mfma_f32_16x16x32_bf16 v[132:135], v[88:91], v[72:75], v[132:135]
	v_mfma_f32_16x16x32_bf16 v[136:139], v[100:103], v[76:79], v[132:135]
